# LN1 row loop waits only for the row loads (not the previous row's store acks); expert GEMM 1 next-unit token-list loads batched (one wait instead of three)
# baseline (speedup 1.0000x reference)
; __device__ __forceinline__ void ph_ln1(const Params& p, int l, LAS unsigned char* lds, const int wvid) {
;     ...
;     __syncthreads();
;     for (int i = tid; i < D * NE / 4; i += NTHR) { const f32x4 w = *(const f32x4*)(p.in[I_ROUTW] + 4 * i); const int c = i >> 2, e0 = (i & 3) * 4;
;         rw[(e0 + 0) * D + c] = w[0]; rw[(e0 + 1) * D + c] = w[1]; rw[(e0 + 2) * D + c] = w[2]; rw[(e0 + 3) * D + c] = w[3]; }
;     if (tid < 16) lcnt[tid] = 0;
;     __syncthreads();
;     const bf16_t* Z = (const bf16_t*)(ws + WS_Z); bf16_t* HB = (bf16_t*)(ws + WS_HB);
;     unsigned* cnt = (unsigned*)(ws + WS_CTL) + CW_CNT + l * 16;
;     int* TE = (int*)(ws + WS_TOKE); int* TP = (int*)(ws + WS_TOKP);
;     const LnPar ln1 = ln_par(p.in[I_LN1G] + l * D, p.in[I_LN1B] + l * D, lane);
;     int k = 0;
;     u32x2 zn[4];
; #pragma unroll
;     for (int j = 0; j < 4; ++j) zn[j] = *(const u32x2*)(Z + (size_t)min(gw, T - 1) * D + 4 * lane + 256 * j);
.LBB0_1069:
	s_or_b64 exec, exec, s[0:1]
	v_cmp_gt_i32_e64 s[2:3], 16, v38
	v_lshl_add_u32 v84, v38, 2, 0
	s_and_saveexec_b64 s[0:1], s[2:3]
	v_add_u32_e32 v0, 0x10000, v84
	ds_write_b32 v0, v1
	s_or_b64 exec, exec, s[0:1]
	v_ashrrev_i32_e32 v41, 6, v38
	v_lshl_add_u32 v42, s4, 3, v41
	s_mov_b32 s0, 0x8080
	v_and_b32_e32 v40, 63, v34
	v_cmp_gt_i32_e32 vcc, s0, v42
	v_mov_b32_e32 v4, 0
	v_mov_b32_e32 v0, 0
	s_waitcnt lgkmcnt(0)
	s_barrier
	s_and_saveexec_b64 s[20:21], vcc
	s_cbranch_execz .LBB0_1131
	v_readlane_b32 s4, v255, 12
	s_add_u32 s0, s18, 0x4090000
	v_readlane_b32 s5, v255, 13
	v_readlane_b32 s48, v253, 62
	s_addc_u32 s1, s19, 0
	s_lshl_b64 s[4:5], s[4:5], 2
	v_readlane_b32 s58, v254, 8
	v_readlane_b32 s59, v254, 9
	s_add_u32 s6, s58, s4
	v_readlane_b32 s56, v254, 6
	s_addc_u32 s7, s59, s5
	v_readlane_b32 s57, v254, 7
	v_lshlrev_b32_e32 v36, 4, v40
	s_add_u32 s4, s56, s4
	s_addc_u32 s5, s57, s5
	global_load_dwordx4 v[2:5], v36, s[6:7] offset:3072
	global_load_dwordx4 v[6:9], v36, s[6:7] offset:2048
	global_load_dwordx4 v[10:13], v36, s[4:5] offset:3072
	global_load_dwordx4 v[14:17], v36, s[4:5] offset:2048
	global_load_dwordx4 v[18:21], v36, s[6:7] offset:1024
	global_load_dwordx4 v[22:25], v36, s[6:7]
	global_load_dwordx4 v[26:29], v36, s[4:5] offset:1024
	global_load_dwordx4 v[30:33], v36, s[4:5]
	v_ashrrev_i32_e32 v43, 31, v42
	v_lshlrev_b64 v[58:59], 11, v[42:43]
	v_lshlrev_b32_e32 v0, 3, v40
	v_lshl_add_u64 v[44:45], s[0:1], 0, v[58:59]
	v_lshl_add_u64 v[44:45], v[44:45], 0, v[0:1]
	global_load_dwordx2 v[56:57], v[44:45], off offset:1536
	global_load_dwordx2 v[54:55], v[44:45], off offset:1024
	global_load_dwordx2 v[52:53], v[44:45], off offset:512
	global_load_dwordx2 v[50:51], v[44:45], off
	v_lshl_add_u64 v[44:45], s[0:1], 0, v[0:1]
	v_lshl_add_u64 v[46:47], s[18:19], 0, v[0:1]
	v_and_b32_e32 v0, 8, v34
	v_cmp_eq_u32_e32 vcc, 0, v0
	v_and_b32_e32 v0, 4, v34
	v_cmp_eq_u32_e64 s[4:5], 0, v0
	v_and_b32_e32 v0, 2, v34
	s_mov_b64 s[0:1], 0x10000
	v_mov_b32_e32 v37, v1
	v_cmp_eq_u32_e64 s[6:7], 0, v0
	v_and_b32_e32 v0, 1, v34
	v_and_b32_e32 v34, 64, v222
	v_lshl_add_u64 v[46:47], v[46:47], 0, s[0:1]
	v_lshl_add_u64 v[48:49], s[18:19], 0, v[36:37]
	s_mov_b64 s[0:1], 0x9090000
	v_cmp_eq_u32_e64 s[8:9], 0, v0
	v_xor_b32_e32 v0, 16, v222
	v_add_u32_e32 v34, 64, v34
	v_lshl_add_u64 v[48:49], v[48:49], 0, s[0:1]
	v_cmp_lt_i32_e64 s[0:1], v0, v34
	v_lshl_or_b32 v58, v40, 3, v58
	v_add_u32_e32 v39, 0, v36
	v_cndmask_b32_e64 v0, v222, v0, s[0:1]
	v_lshlrev_b32_e32 v43, 2, v0
	v_xor_b32_e32 v0, 32, v222
	v_cmp_lt_i32_e64 s[0:1], v0, v34
	v_lshl_add_u64 v[34:35], s[18:19], 0, v[58:59]
	s_mov_b32 s24, -1
	v_cndmask_b32_e64 v0, v222, v0, s[0:1]
	s_movk_i32 s0, 0x500
	v_lshlrev_b32_e32 v85, 2, v0
	v_mul_lo_u32 v0, v41, s0
	v_lshl_or_b32 v0, v40, 2, v0
	v_readlane_b32 s0, v254, 28
	v_cmp_gt_u32_e64 s[10:11], 16, v40
	s_mov_b64 s[16:17], 0
	v_add_u32_e32 v86, s0, v0
	s_mov_b64 s[0:1], 0x10600
	v_lshl_add_u64 v[58:59], v[34:35], 0, s[0:1]
	v_mov_b32_e32 v34, v42
	v_readlane_b32 s49, v253, 63
	v_readlane_b32 s50, v254, 0
	v_readlane_b32 s51, v254, 1
	v_readlane_b32 s52, v254, 2
	v_readlane_b32 s53, v254, 3
	v_readlane_b32 s54, v254, 4
	v_readlane_b32 s55, v254, 5
	v_readlane_b32 s60, v254, 10
	v_readlane_b32 s61, v254, 11
	v_readlane_b32 s62, v254, 12
	v_readlane_b32 s63, v254, 13
	s_waitcnt vmcnt(0)
	s_branch .LBB0_1074

; __device__ __forceinline__ float bflo(unsigned w) { return __uint_as_float(w << 16); }
; __device__ __forceinline__ float bfhi(unsigned w) { return __uint_as_float(w & 0xFFFF0000u); }
; __device__ __forceinline__ void ph_ln1(const Params& p, int l, LAS unsigned char* lds, const int wvid) {
;     ...
;     for (int r = gw; r < T; r += NGW, ++k) {
;         f32x4 v[4]; u32x2 zc[4];
; #pragma unroll
;         for (int j = 0; j < 4; ++j) { zc[j] = zn[j]; zn[j] = *(const u32x2*)(Z + (size_t)min(r + NGW, T - 1) * D + 4 * lane + 256 * j); }
;         if (r < MP - 256) {
; #pragma unroll
;             for (int j = 0; j < 4; ++j) { const u32x2 z = zc[j]; v[j] = (f32x4){bflo(z.x), bfhi(z.x), bflo(z.y), bfhi(z.y)}; }
;         } else {
;             const float* zp = (const float*)(ws + WS_ZP) + (size_t)(r - (MP - 256)) * D + 4 * lane;
; #pragma unroll
;             for (int j = 0; j < 4; ++j) { const u32x2 hh = *(const u32x2*)(HB + (size_t)r * D + 4 * lane + 256 * j); f32x4 a = (f32x4){ALPHA * bflo(hh.x), ALPHA * bfhi(hh.x), ALPHA * bflo(hh.y), ALPHA * bfhi(hh.y)};
; #pragma unroll
;                 for (int k2 = 0; k2 < ZSPLIT; ++k2) a = a + *(const f32x4*)(zp + (size_t)k2 * 256 * D + 256 * j);
;                 v[j] = a; }
;         }
.LBB0_1074:
	v_add_u32_e32 v87, s80, v34
	v_min_i32_e32 v36, 0x807f, v87
	v_ashrrev_i32_e32 v37, 31, v36
	v_lshlrev_b64 v[36:37], 11, v[36:37]
	v_lshl_add_u64 v[36:37], v[44:45], 0, v[36:37]
	s_waitcnt vmcnt(4)
	v_mov_b64_e32 v[64:65], v[56:57]
	v_mov_b64_e32 v[70:71], v[54:55]
	v_mov_b64_e32 v[80:81], v[52:53]
	v_mov_b64_e32 v[82:83], v[50:51]
	global_load_dwordx2 v[50:51], v[36:37], off
	global_load_dwordx2 v[52:53], v[36:37], off offset:512
	global_load_dwordx2 v[54:55], v[36:37], off offset:1024
	global_load_dwordx2 v[56:57], v[36:37], off offset:1536
	v_cmp_lt_i32_e64 s[0:1], s79, v34
	s_and_saveexec_b64 s[22:23], s[0:1]
	s_xor_b64 s[22:23], exec, s[22:23]
	s_cbranch_execz .LBB0_1076
	v_mov_b32_e32 v35, v1
	v_add_u32_e32 v0, 0xffff8000, v34
	v_lshlrev_b64 v[34:35], 11, v[34:35]
	v_lshl_add_u64 v[76:77], v[46:47], 0, v[34:35]
	global_load_dwordx2 v[34:35], v[76:77], off
	v_lshlrev_b64 v[36:37], 12, v[0:1]
	v_lshl_add_u64 v[74:75], v[48:49], 0, v[36:37]
	s_mov_b32 s0, 0x100000
	v_add_co_u32_e64 v184, s[0:1], s0, v74
	s_nop 1
	v_addc_co_u32_e64 v185, s[0:1], 0, v75, s[0:1]
	s_mov_b32 s0, 0x200000
	s_nop 0
	v_add_co_u32_e64 v186, s[0:1], s0, v74
	s_nop 1
	v_addc_co_u32_e64 v187, s[0:1], 0, v75, s[0:1]
	s_mov_b32 s0, 0x300000
	s_nop 0
	v_add_co_u32_e64 v188, s[0:1], s0, v74
	s_nop 1
	v_addc_co_u32_e64 v189, s[0:1], 0, v75, s[0:1]
	global_load_dwordx4 v[118:121], v[74:75], off
	global_load_dwordx4 v[122:125], v[184:185], off
	global_load_dwordx4 v[126:129], v[186:187], off
	global_load_dwordx4 v[130:133], v[188:189], off
	global_load_dwordx2 v[88:89], v[76:77], off offset:512
	global_load_dwordx4 v[134:137], v[74:75], off offset:1024
	global_load_dwordx4 v[138:141], v[184:185], off offset:1024
	global_load_dwordx4 v[142:145], v[186:187], off offset:1024
	global_load_dwordx4 v[146:149], v[188:189], off offset:1024
	global_load_dwordx2 v[90:91], v[76:77], off offset:1024
	global_load_dwordx2 v[92:93], v[76:77], off offset:1536
	global_load_dwordx4 v[232:235], v[74:75], off offset:2048
	global_load_dwordx4 v[236:239], v[184:185], off offset:2048
	global_load_dwordx4 v[240:243], v[186:187], off offset:2048
	global_load_dwordx4 v[244:247], v[188:189], off offset:2048
	global_load_dwordx4 v[196:199], v[74:75], off offset:3072
	global_load_dwordx4 v[200:203], v[184:185], off offset:3072
	global_load_dwordx4 v[206:209], v[186:187], off offset:3072
	global_load_dwordx4 v[210:213], v[188:189], off offset:3072
	s_mov_b32 s0, 0x100000
	v_add_co_u32_e64 v72, s[0:1], s0, v74
	s_waitcnt vmcnt(0)
	v_lshlrev_b32_e32 v60, 16, v34
	v_and_b32_e32 v61, 0xffff0000, v34
	v_lshlrev_b32_e32 v62, 16, v35
	v_and_b32_e32 v63, 0xffff0000, v35
	v_mov_b64_e32 v[34:35], v[118:119]
	v_mov_b64_e32 v[36:37], v[120:121]
	v_addc_co_u32_e64 v73, s[0:1], 0, v75, s[0:1]
	s_mov_b32 s0, 0x200000
	s_nop 0
	v_add_co_u32_e64 v70, s[0:1], s0, v74
	s_waitcnt vmcnt(0)
	v_pk_fma_f32 v[60:61], v[60:61], s[88:89], v[34:35] op_sel_hi:[1,0,1]
	v_pk_fma_f32 v[62:63], v[62:63], s[88:89], v[36:37] op_sel_hi:[1,0,1]
	v_mov_b64_e32 v[34:35], v[122:123]
	v_mov_b64_e32 v[36:37], v[124:125]
	v_addc_co_u32_e64 v71, s[0:1], 0, v75, s[0:1]
	s_mov_b32 s0, 0x300000
	s_nop 0
	v_add_co_u32_e64 v68, s[0:1], s0, v74
	s_waitcnt vmcnt(0)
	v_pk_add_f32 v[62:63], v[36:37], v[62:63]
	v_pk_add_f32 v[60:61], v[34:35], v[60:61]
	v_mov_b64_e32 v[34:35], v[126:127]
	v_mov_b64_e32 v[36:37], v[128:129]
	v_addc_co_u32_e64 v69, s[0:1], 0, v75, s[0:1]
	s_waitcnt vmcnt(0)
	v_pk_add_f32 v[36:37], v[36:37], v[62:63]
	v_pk_add_f32 v[64:65], v[34:35], v[60:61]
	v_mov_b64_e32 v[60:61], v[130:131]
	v_mov_b64_e32 v[62:63], v[132:133]
	s_waitcnt vmcnt(0)
	v_pk_add_f32 v[34:35], v[62:63], v[36:37]
	v_mov_b64_e32 v[36:37], v[88:89]
	v_pk_add_f32 v[64:65], v[60:61], v[64:65]
	v_mov_b64_e32 v[60:61], v[134:135]
	v_mov_b64_e32 v[62:63], v[136:137]
	s_waitcnt vmcnt(1)
	v_lshlrev_b32_e32 v66, 16, v36
	v_and_b32_e32 v67, 0xffff0000, v36
	v_lshlrev_b32_e32 v36, 16, v37
	v_and_b32_e32 v37, 0xffff0000, v37
	s_waitcnt vmcnt(0)
	v_pk_fma_f32 v[66:67], v[66:67], s[88:89], v[60:61] op_sel_hi:[1,0,1]
	v_pk_fma_f32 v[36:37], v[36:37], s[88:89], v[62:63] op_sel_hi:[1,0,1]
	v_mov_b64_e32 v[60:61], v[138:139]
	v_mov_b64_e32 v[62:63], v[140:141]
	s_waitcnt vmcnt(0)
	v_pk_add_f32 v[36:37], v[62:63], v[36:37]
	v_pk_add_f32 v[66:67], v[60:61], v[66:67]
	v_mov_b64_e32 v[60:61], v[142:143]
	v_mov_b64_e32 v[62:63], v[144:145]
	s_waitcnt vmcnt(0)
	v_pk_add_f32 v[36:37], v[62:63], v[36:37]
	v_pk_add_f32 v[66:67], v[60:61], v[66:67]
	v_mov_b64_e32 v[60:61], v[146:147]
	v_mov_b64_e32 v[62:63], v[148:149]
	s_waitcnt vmcnt(0)
	v_pk_add_f32 v[66:67], v[60:61], v[66:67]
	v_mov_b64_e32 v[60:61], v[90:91]
	v_pk_add_f32 v[36:37], v[62:63], v[36:37]
	v_mov_b64_e32 v[76:77], v[92:93]
	s_waitcnt vmcnt(1)
	v_lshlrev_b32_e32 v78, 16, v60
	v_and_b32_e32 v79, 0xffff0000, v60
	v_lshlrev_b32_e32 v80, 16, v61
	v_and_b32_e32 v81, 0xffff0000, v61
	v_mov_b64_e32 v[60:61], v[232:233]
	v_mov_b64_e32 v[62:63], v[234:235]
	s_waitcnt vmcnt(0)
	v_pk_fma_f32 v[78:79], v[78:79], s[88:89], v[60:61] op_sel_hi:[1,0,1]
	v_pk_fma_f32 v[80:81], v[80:81], s[88:89], v[62:63] op_sel_hi:[1,0,1]
	v_mov_b64_e32 v[60:61], v[236:237]
	v_mov_b64_e32 v[62:63], v[238:239]
	s_waitcnt vmcnt(0)
	v_pk_add_f32 v[80:81], v[62:63], v[80:81]
	v_pk_add_f32 v[78:79], v[60:61], v[78:79]
	v_mov_b64_e32 v[60:61], v[240:241]
	v_mov_b64_e32 v[62:63], v[242:243]
	s_waitcnt vmcnt(0)
	v_pk_add_f32 v[62:63], v[62:63], v[80:81]
	v_pk_add_f32 v[82:83], v[60:61], v[78:79]
	v_mov_b64_e32 v[78:79], v[244:245]
	v_mov_b64_e32 v[80:81], v[246:247]
	s_waitcnt vmcnt(0)
	v_pk_add_f32 v[60:61], v[80:81], v[62:63]
	v_pk_add_f32 v[62:63], v[78:79], v[82:83]
	v_lshlrev_b32_e32 v78, 16, v76
	v_and_b32_e32 v79, 0xffff0000, v76
	v_lshlrev_b32_e32 v80, 16, v77
	v_and_b32_e32 v81, 0xffff0000, v77
	v_mov_b64_e32 v[74:75], v[196:197]
	v_mov_b64_e32 v[76:77], v[198:199]
	s_waitcnt vmcnt(0)
	v_pk_fma_f32 v[78:79], v[78:79], s[88:89], v[74:75] op_sel_hi:[1,0,1]
	v_mov_b64_e32 v[72:73], v[200:201]
	v_mov_b64_e32 v[74:75], v[202:203]
	v_pk_fma_f32 v[76:77], v[80:81], s[88:89], v[76:77] op_sel_hi:[1,0,1]
	s_waitcnt vmcnt(0)
	v_pk_add_f32 v[74:75], v[74:75], v[76:77]
	v_pk_add_f32 v[76:77], v[72:73], v[78:79]
	v_mov_b64_e32 v[70:71], v[206:207]
	v_mov_b64_e32 v[72:73], v[208:209]
	s_waitcnt vmcnt(0)
	v_pk_add_f32 v[72:73], v[72:73], v[74:75]
	v_pk_add_f32 v[74:75], v[70:71], v[76:77]
	v_mov_b64_e32 v[68:69], v[210:211]
	v_mov_b64_e32 v[70:71], v[212:213]
	s_waitcnt vmcnt(0)
	v_pk_add_f32 v[72:73], v[70:71], v[72:73]
	v_pk_add_f32 v[74:75], v[68:69], v[74:75]
	v_mov_b32_e32 v76, v73
	v_mov_b32_e32 v78, v75
	v_mov_b32_e32 v69, v36
	v_mov_b32_e32 v68, v67
	v_mov_b32_e32 v36, v66
	v_mov_b32_e32 v67, v34
	v_mov_b32_e32 v66, v65
	v_mov_b32_e32 v34, v64

; #define PG8_STAGE(bufoff, gbase, voff) do { _Pragma("unroll") for (int _i = 0; _i < 2; ++_i) \
;         __builtin_amdgcn_global_load_lds((const unsigned*)((const char*)(gbase) + (voff)[_i]), (LAS unsigned*)(lds + (bufoff) + ldsw + _i * 8192), 16, 0, 0); } while (0)
; #define PG8_LDA(dst, b, h) do { _Pragma("unroll") for (int m = 0; m < 4; ++m) _Pragma("unroll") for (int k = 0; k < 2; ++k) dst[m][k] = *(const LAS bf16x8*)(lds + PG8_SA(b, h) + aoff + m * 2048 + k * 1024); } while (0)
; #define PG8_LDB(dst, b, h) do { _Pragma("unroll") for (int n = 0; n < 2; ++n) _Pragma("unroll") for (int k = 0; k < 2; ++k) dst[n][k] = *(const LAS bf16x8*)(lds + PG8_SB(b, h) + boff + n * 2048 + k * 1024); } while (0)
; #define PG8_MMA(ai, bj, At, Bt) do { __builtin_amdgcn_s_setprio(1); _Pragma("unroll") for (int m = 0; m < 4; ++m) _Pragma("unroll") for (int n = 0; n < 2; ++n) _Pragma("unroll") for (int k = 0; k < 2; ++k) \
;         acc[ai][bj][m][n] = __builtin_amdgcn_mfma_f32_16x16x32_bf16(Bt[n][k], At[m][k], acc[ai][bj][m][n], 0, 0, 0); __builtin_amdgcn_s_setprio(0); } while (0)
; #define PG8_WAIT_L(n) asm volatile("s_waitcnt lgkmcnt(" #n ")" ::: "memory")
; #define PG8_BAR __builtin_amdgcn_s_barrier()
; #define PG8_SCHED __builtin_amdgcn_sched_barrier(0)
; #define PG8_AOFF(u) do { const int _t = lt_tid(wvid); _Pragma("unroll") for (int _i = 0; _i < 2; ++_i) { int _R, _C; stage_rc(_t * 16 + _i * 8192, _R, _C); \
;         _Pragma("unroll") for (int _h = 0; _h < 2; ++_h) voffA[_h][_i] = (S.a_row(u, _h * HALF + _R) * (unsigned)K + (unsigned)(_C + (u).koff)) * 2u; } } while (0)
; template <class Epi, class Sched>
; __device__ __forceinline__ void gemm_phase(LAS unsigned char* lds, const bf16_t* Abase, const int K, const Sched& S, const Epi& E, const int wvid) {
;     ...
;             PG8_LDB(B0, 0, 0); PG8_SCHED; PG8_LDA(At, 0, 0); PG8_STAGE(PG8_SA(1, 1), a1, voffA[1]);
;             PG8_WAIT_L(8); PG8_BAR; PG8_WAIT_L(0); PG8_MMA(0, 0, At, B0); PG8_BAR; PG8_SCHED;
;             if (last && has_next) PG8_AOFF(nxt);
.LBB0_1209:
	v_add_u32_e32 v130, 0, v224
	v_add_u32_e32 v142, 0x10000, v130
	ds_read_b128 v[130:133], v142
	ds_read_b128 v[134:137], v142 offset:1024
	ds_read_b128 v[138:141], v142 offset:2048
	ds_read_b128 v[142:145], v142 offset:3072
	s_cmp_eq_u32 s23, 12
	s_cselect_b64 s[4:5], -1, 0
	s_add_i32 m0, s25, 0xc000
	s_add_u32 s28, s20, s26
	s_addc_u32 s29, s21, s27
	ds_read_b128 v[170:173], v226
	ds_read_b128 v[174:177], v226 offset:1024
	ds_read_b128 v[162:165], v226 offset:2048
	ds_read_b128 v[166:169], v226 offset:3072
	ds_read_b128 v[154:157], v226 offset:4096
	ds_read_b128 v[158:161], v226 offset:5120
	ds_read_b128 v[146:149], v226 offset:6144
	ds_read_b128 v[150:153], v226 offset:7168
	global_load_lds_dwordx4 v186, s[28:29]
	s_add_i32 m0, s25, 0xe000
	s_nop 0
	global_load_lds_dwordx4 v188, s[28:29]
	s_waitcnt lgkmcnt(8)
	s_barrier
	s_waitcnt lgkmcnt(0)
	s_setprio 1
	s_waitcnt lgkmcnt(0)
	v_mfma_f32_16x16x32_bf16 v[126:129], v[130:133], v[170:173], v[126:129]
	v_mfma_f32_16x16x32_bf16 v[122:125], v[138:141], v[170:173], v[122:125]
	v_mfma_f32_16x16x32_bf16 v[118:121], v[130:133], v[162:165], v[118:121]
	v_mfma_f32_16x16x32_bf16 v[114:117], v[138:141], v[162:165], v[114:117]
	v_mfma_f32_16x16x32_bf16 v[110:113], v[130:133], v[154:157], v[110:113]
	v_mfma_f32_16x16x32_bf16 v[106:109], v[138:141], v[154:157], v[106:109]
	v_mfma_f32_16x16x32_bf16 v[94:97], v[130:133], v[146:149], v[94:97]
	v_mfma_f32_16x16x32_bf16 v[90:93], v[138:141], v[146:149], v[90:93]
	v_mfma_f32_16x16x32_bf16 v[126:129], v[134:137], v[174:177], v[126:129]
	v_mfma_f32_16x16x32_bf16 v[122:125], v[142:145], v[174:177], v[122:125]
	v_mfma_f32_16x16x32_bf16 v[118:121], v[134:137], v[166:169], v[118:121]
	v_mfma_f32_16x16x32_bf16 v[114:117], v[142:145], v[166:169], v[114:117]
	v_mfma_f32_16x16x32_bf16 v[110:113], v[134:137], v[158:161], v[110:113]
	v_mfma_f32_16x16x32_bf16 v[106:109], v[142:145], v[158:161], v[106:109]
	v_mfma_f32_16x16x32_bf16 v[94:97], v[134:137], v[150:153], v[94:97]
	v_mfma_f32_16x16x32_bf16 v[90:93], v[142:145], v[150:153], v[90:93]
	s_setprio 0
	s_barrier
	s_and_b64 s[28:29], s[0:1], s[4:5]
	s_andn2_b64 vcc, exec, s[28:29]
	s_cbranch_vccnz .LBB0_1211
	v_mbcnt_lo_u32_b32 v0, -1, 0
	v_mbcnt_hi_u32_b32 v0, -1, v0
	v_mov_b32_e32 v189, v1
	v_or_b32_e32 v0, s75, v0
	v_ashrrev_i32_e32 v184, 31, v0
	v_lshrrev_b32_e32 v184, 26, v184
	v_lshlrev_b32_e32 v186, 4, v0
	v_add_u32_e32 v184, v0, v184
	v_bfe_i32 v0, v0, 27, 1
	v_lshrrev_b32_e32 v0, 22, v0
	v_add_u32_e32 v0, v186, v0
	v_and_b32_e32 v0, 0xfffffc00, v0
	v_sub_u32_e32 v0, v186, v0
	v_lshrrev_b32_e32 v185, 4, v0
	v_bitop3_b32 v0, v185, v0, 32 bitop3:0x6c
	v_ashrrev_i32_e32 v187, 31, v0
	v_ashrrev_i32_e32 v184, 6, v184
	v_lshrrev_b32_e32 v187, 26, v187
	v_lshlrev_b32_e32 v185, 3, v184
	v_add_u32_e32 v187, v0, v187
	v_and_b32_e32 v185, -16, v185
	v_ashrrev_i32_e32 v188, 6, v187
	v_add_u32_e32 v188, v188, v185
	v_and_b32_e32 v185, 0xc0, v187
	v_sub_u32_e32 v0, v0, v185
	v_lshlrev_b32_e32 v184, 5, v184
	v_ashrrev_i16_sdwa v0, v216, sext(v0) dst_sel:DWORD dst_unused:UNUSED_PAD src0_sel:DWORD src1_sel:BYTE_0
	v_and_b32_e32 v184, 32, v184
	v_bfe_i32 v0, v0, 0, 16
	v_add_lshl_u32 v0, v184, v0, 1
	v_add_u32_e32 v232, v188, v227
	v_min_i32_e32 v232, v232, v230
	v_add_u32_e32 v232, v232, v192
	v_ashrrev_i32_e32 v233, 31, v232
	v_lshl_add_u64 v[232:233], v[232:233], 2, s[10:11]
	global_load_dword v240, v[232:233], off
	v_add_u32_e32 v234, v188, v231
	v_min_i32_e32 v234, v234, v230
	v_add_u32_e32 v234, v234, v192
	v_ashrrev_i32_e32 v235, 31, v234
	v_lshl_add_u64 v[234:235], v[234:235], 2, s[10:11]
	global_load_dword v241, v[234:235], off
	v_add_u32_e32 v184, 0x2000, v186
	v_ashrrev_i32_e32 v185, 31, v184
	v_lshrrev_b32_e32 v185, 22, v185
	v_add_u32_e32 v185, v184, v185
	v_ashrrev_i32_e32 v185, 10, v185
	v_mul_i32_i24_e32 v186, 0x400, v185
	v_sub_u32_e32 v184, v184, v186
	v_lshrrev_b32_e32 v186, 4, v184
	v_bitop3_b32 v184, v186, v184, 32 bitop3:0x6c
	v_ashrrev_i32_e32 v187, 31, v184
	v_lshrrev_b32_e32 v187, 26, v187
	v_add_u32_e32 v187, v184, v187
	v_ashrrev_i32_e32 v188, 6, v187
	v_and_b32_e32 v187, 0xc0, v187
	v_lshlrev_b32_e32 v186, 3, v185
	v_sub_u32_e32 v184, v184, v187
	v_and_b32_e32 v186, -16, v186
	v_lshlrev_b32_e32 v185, 5, v185
	v_ashrrev_i16_sdwa v184, v216, sext(v184) dst_sel:DWORD dst_unused:UNUSED_PAD src0_sel:DWORD src1_sel:BYTE_0
	v_add_u32_e32 v186, v188, v186
	v_and_b32_e32 v185, 32, v185
	v_bfe_i32 v184, v184, 0, 16
	v_add_lshl_u32 v188, v185, v184, 1
	v_add_u32_e32 v236, v186, v227
	v_min_i32_e32 v236, v236, v230
	v_add_u32_e32 v236, v236, v192
	v_ashrrev_i32_e32 v237, 31, v236
	v_lshl_add_u64 v[236:237], v[236:237], 2, s[10:11]
	global_load_dword v242, v[236:237], off
	v_add_u32_e32 v238, v186, v231
	v_min_i32_e32 v238, v238, v230
	v_add_u32_e32 v238, v238, v192
	v_ashrrev_i32_e32 v239, 31, v238
	v_lshl_add_u64 v[238:239], v[238:239], 2, s[10:11]
	global_load_dword v243, v[238:239], off
	s_waitcnt vmcnt(0)
	v_lshl_add_u32 v200, v240, 11, v0
	v_lshl_add_u32 v0, v241, 11, v0
	v_mov_b64_e32 v[198:199], v[0:1]
	v_mov_b32_e32 v186, v0
	v_mov_b32_e32 v0, v200
	v_lshl_add_u32 v184, v242, 11, v188
	v_lshl_add_u32 v188, v243, 11, v188
	s_branch .LBB0_1212
